# same as the compact-mask-loop version with the unreachable dilated-attention edge-mask code deleted
# baseline (speedup 1.0000x reference)
.LBB0_1560:
	s_cmp_eq_u32 s63, 3
	s_cselect_b64 s[12:13], -1, 0
	s_cmp_eq_u32 s62, 3
	s_cselect_b64 s[46:47], -1, 0
	s_and_b64 s[12:13], s[12:13], s[46:47]
	s_and_b64 vcc, exec, s[12:13]
	s_cbranch_vccnz .LBB0_1566
	s_lshl_b32 s12, s61, 6
	s_add_i32 s12, s12, s51
	s_lshl_b32 s12, s12, 2
	v_subrev_u32_e32 v2, s12, v143
	ds_read2_b32 v[146:147], v2 offset0:127 offset1:128
	s_or_b32 s12, s62, s63
	s_cmp_eq_u32 s12, 0
	s_waitcnt lgkmcnt(0)
	v_pk_add_f32 v[68:69], v[68:69], v[146:147] op_sel:[0,1] op_sel_hi:[1,0]
	ds_read2_b32 v[146:147], v2 offset0:95 offset1:96
	s_waitcnt lgkmcnt(0)
	v_pk_add_f32 v[36:37], v[36:37], v[146:147] op_sel:[0,1] op_sel_hi:[1,0]
	ds_read2_b32 v[146:147], v2 offset0:125 offset1:126
	s_waitcnt lgkmcnt(0)
	v_pk_add_f32 v[70:71], v[70:71], v[146:147] op_sel:[0,1] op_sel_hi:[1,0]
	ds_read2_b32 v[146:147], v2 offset0:93 offset1:94
	s_waitcnt lgkmcnt(0)
	v_pk_add_f32 v[38:39], v[38:39], v[146:147] op_sel:[0,1] op_sel_hi:[1,0]
	ds_read2_b32 v[146:147], v2 offset0:119 offset1:120
	s_waitcnt lgkmcnt(0)
	v_pk_add_f32 v[72:73], v[72:73], v[146:147] op_sel:[0,1] op_sel_hi:[1,0]
	ds_read2_b32 v[146:147], v2 offset0:87 offset1:88
	s_waitcnt lgkmcnt(0)
	v_pk_add_f32 v[40:41], v[40:41], v[146:147] op_sel:[0,1] op_sel_hi:[1,0]
	ds_read2_b32 v[146:147], v2 offset0:117 offset1:118
	s_waitcnt lgkmcnt(0)
	v_pk_add_f32 v[74:75], v[74:75], v[146:147] op_sel:[0,1] op_sel_hi:[1,0]
	ds_read2_b32 v[146:147], v2 offset0:85 offset1:86
	s_waitcnt lgkmcnt(0)
	v_pk_add_f32 v[42:43], v[42:43], v[146:147] op_sel:[0,1] op_sel_hi:[1,0]
	ds_read2_b32 v[146:147], v2 offset0:111 offset1:112
	s_waitcnt lgkmcnt(0)
	v_pk_add_f32 v[76:77], v[76:77], v[146:147] op_sel:[0,1] op_sel_hi:[1,0]
	ds_read2_b32 v[146:147], v2 offset0:79 offset1:80
	s_waitcnt lgkmcnt(0)
	v_pk_add_f32 v[44:45], v[44:45], v[146:147] op_sel:[0,1] op_sel_hi:[1,0]
	ds_read2_b32 v[146:147], v2 offset0:109 offset1:110
	s_waitcnt lgkmcnt(0)
	v_pk_add_f32 v[78:79], v[78:79], v[146:147] op_sel:[0,1] op_sel_hi:[1,0]
	ds_read2_b32 v[146:147], v2 offset0:77 offset1:78
	s_waitcnt lgkmcnt(0)
	v_pk_add_f32 v[46:47], v[46:47], v[146:147] op_sel:[0,1] op_sel_hi:[1,0]
	ds_read2_b32 v[146:147], v2 offset0:103 offset1:104
	s_waitcnt lgkmcnt(0)
	v_pk_add_f32 v[80:81], v[80:81], v[146:147] op_sel:[0,1] op_sel_hi:[1,0]
	ds_read2_b32 v[146:147], v2 offset0:71 offset1:72
	s_waitcnt lgkmcnt(0)
	v_pk_add_f32 v[48:49], v[48:49], v[146:147] op_sel:[0,1] op_sel_hi:[1,0]
	ds_read2_b32 v[146:147], v2 offset0:101 offset1:102
	s_waitcnt lgkmcnt(0)
	v_pk_add_f32 v[82:83], v[82:83], v[146:147] op_sel:[0,1] op_sel_hi:[1,0]
	ds_read2_b32 v[146:147], v2 offset0:69 offset1:70
	s_waitcnt lgkmcnt(0)
	v_pk_add_f32 v[50:51], v[50:51], v[146:147] op_sel:[0,1] op_sel_hi:[1,0]
.LBB0_1563:
	v_max3_f32 v2, v68, v69, v36
	v_max3_f32 v146, v70, v71, v37
	s_nop 0
	v_max3_f32 v2, v2, v38, v39
	v_max3_f32 v146, v146, v74, v75
	s_nop 0
	v_max3_f32 v2, v2, v72, v73
	v_max3_f32 v146, v146, v42, v43
	s_nop 0
	v_max3_f32 v2, v2, v40, v41
	v_max3_f32 v146, v146, v78, v79
	s_nop 0
	v_max3_f32 v2, v2, v76, v77
	v_max3_f32 v146, v146, v46, v47
	s_nop 0
	v_max3_f32 v2, v2, v44, v45
	v_max3_f32 v146, v146, v82, v83
	s_nop 0
	v_max3_f32 v2, v2, v80, v81
	v_max3_f32 v146, v146, v50, v51
	s_nop 0
	v_max3_f32 v2, v2, v48, v49
	s_nop 0
	v_max3_f32 v2, v2, v146, v146
	s_nop 0
	v_mov_b32_e32 v146, v2
	s_nop 1
	v_permlane32_swap_b32_e32 v2, v146
	v_max_f32_e32 v146, v146, v146
	v_max_f32_e32 v2, v2, v2
	v_max_f32_e32 v2, v2, v146
	v_add_f32_e32 v146, 0x40c00000, v145
	v_add_f32_e32 v147, 0, v2
	v_cmp_gt_f32_e32 vcc, v2, v146
	s_nop 1
	v_cndmask_b32_e32 v2, v145, v147, vcc
	v_cmp_gt_f32_e32 vcc, v2, v145
	s_cbranch_vccz .LBB0_1565
	v_sub_f32_e32 v145, v145, v2
	v_exp_f32_e32 v146, v145
	s_nop 0
	v_pk_mul_f32 v[66:67], v[66:67], v[146:147] op_sel_hi:[1,0]
	v_pk_mul_f32 v[64:65], v[64:65], v[146:147] op_sel_hi:[1,0]
	v_pk_mul_f32 v[62:63], v[62:63], v[146:147] op_sel_hi:[1,0]
	v_pk_mul_f32 v[60:61], v[60:61], v[146:147] op_sel_hi:[1,0]
	v_pk_mul_f32 v[58:59], v[58:59], v[146:147] op_sel_hi:[1,0]
	v_pk_mul_f32 v[56:57], v[56:57], v[146:147] op_sel_hi:[1,0]
	v_pk_mul_f32 v[54:55], v[54:55], v[146:147] op_sel_hi:[1,0]
	v_pk_mul_f32 v[52:53], v[52:53], v[146:147] op_sel_hi:[1,0]
	v_pk_mul_f32 v[34:35], v[34:35], v[146:147] op_sel_hi:[1,0]
	v_pk_mul_f32 v[32:33], v[32:33], v[146:147] op_sel_hi:[1,0]
	v_pk_mul_f32 v[30:31], v[30:31], v[146:147] op_sel_hi:[1,0]
	v_pk_mul_f32 v[28:29], v[28:29], v[146:147] op_sel_hi:[1,0]
	v_pk_mul_f32 v[26:27], v[26:27], v[146:147] op_sel_hi:[1,0]
	v_pk_mul_f32 v[24:25], v[24:25], v[146:147] op_sel_hi:[1,0]
	v_pk_mul_f32 v[22:23], v[22:23], v[146:147] op_sel_hi:[1,0]
	v_pk_mul_f32 v[20:21], v[20:21], v[146:147] op_sel_hi:[1,0]
	v_pk_mul_f32 v[18:19], v[18:19], v[146:147] op_sel_hi:[1,0]
	v_pk_mul_f32 v[16:17], v[16:17], v[146:147] op_sel_hi:[1,0]
	v_pk_mul_f32 v[14:15], v[14:15], v[146:147] op_sel_hi:[1,0]
	v_pk_mul_f32 v[12:13], v[12:13], v[146:147] op_sel_hi:[1,0]
	v_pk_mul_f32 v[10:11], v[10:11], v[146:147] op_sel_hi:[1,0]
	v_pk_mul_f32 v[8:9], v[8:9], v[146:147] op_sel_hi:[1,0]
	v_pk_mul_f32 v[6:7], v[6:7], v[146:147] op_sel_hi:[1,0]
	v_pk_mul_f32 v[4:5], v[4:5], v[146:147] op_sel_hi:[1,0]

.LBB0_1588:
	s_cmp_eq_u32 s60, 3
	s_cselect_b64 s[12:13], -1, 0
	s_cmp_eq_u32 s47, 3
	s_cselect_b64 s[40:41], -1, 0
	s_and_b64 s[12:13], s[12:13], s[40:41]
	s_and_b64 vcc, exec, s[12:13]
	s_cbranch_vccnz .LBB0_1594
	s_lshl_b32 s12, s59, 6
	s_add_i32 s12, s12, s51
	s_lshl_b32 s12, s12, 2
	v_subrev_u32_e32 v145, s12, v143
	ds_read2_b32 v[146:147], v145 offset0:127 offset1:128
	s_or_b32 s12, s47, s60
	s_cmp_eq_u32 s12, 0
	s_waitcnt lgkmcnt(0)
	v_pk_add_f32 v[84:85], v[84:85], v[146:147] op_sel:[0,1] op_sel_hi:[1,0]
	ds_read2_b32 v[146:147], v145 offset0:95 offset1:96
	s_waitcnt lgkmcnt(0)
	v_pk_add_f32 v[100:101], v[100:101], v[146:147] op_sel:[0,1] op_sel_hi:[1,0]
	ds_read2_b32 v[146:147], v145 offset0:125 offset1:126
	s_waitcnt lgkmcnt(0)
	v_pk_add_f32 v[86:87], v[86:87], v[146:147] op_sel:[0,1] op_sel_hi:[1,0]
	ds_read2_b32 v[146:147], v145 offset0:93 offset1:94
	s_waitcnt lgkmcnt(0)
	v_pk_add_f32 v[102:103], v[102:103], v[146:147] op_sel:[0,1] op_sel_hi:[1,0]
	ds_read2_b32 v[146:147], v145 offset0:119 offset1:120
	s_waitcnt lgkmcnt(0)
	v_pk_add_f32 v[88:89], v[88:89], v[146:147] op_sel:[0,1] op_sel_hi:[1,0]
	ds_read2_b32 v[146:147], v145 offset0:87 offset1:88
	s_waitcnt lgkmcnt(0)
	v_pk_add_f32 v[104:105], v[104:105], v[146:147] op_sel:[0,1] op_sel_hi:[1,0]
	ds_read2_b32 v[146:147], v145 offset0:117 offset1:118
	s_waitcnt lgkmcnt(0)
	v_pk_add_f32 v[90:91], v[90:91], v[146:147] op_sel:[0,1] op_sel_hi:[1,0]
	ds_read2_b32 v[146:147], v145 offset0:85 offset1:86
	s_waitcnt lgkmcnt(0)
	v_pk_add_f32 v[106:107], v[106:107], v[146:147] op_sel:[0,1] op_sel_hi:[1,0]
	ds_read2_b32 v[146:147], v145 offset0:111 offset1:112
	s_waitcnt lgkmcnt(0)
	v_pk_add_f32 v[92:93], v[92:93], v[146:147] op_sel:[0,1] op_sel_hi:[1,0]
	ds_read2_b32 v[146:147], v145 offset0:79 offset1:80
	s_waitcnt lgkmcnt(0)
	v_pk_add_f32 v[108:109], v[108:109], v[146:147] op_sel:[0,1] op_sel_hi:[1,0]
	ds_read2_b32 v[146:147], v145 offset0:109 offset1:110
	s_waitcnt lgkmcnt(0)
	v_pk_add_f32 v[94:95], v[94:95], v[146:147] op_sel:[0,1] op_sel_hi:[1,0]
	ds_read2_b32 v[146:147], v145 offset0:77 offset1:78
	s_waitcnt lgkmcnt(0)
	v_pk_add_f32 v[110:111], v[110:111], v[146:147] op_sel:[0,1] op_sel_hi:[1,0]
	ds_read2_b32 v[146:147], v145 offset0:103 offset1:104
	s_waitcnt lgkmcnt(0)
	v_pk_add_f32 v[96:97], v[96:97], v[146:147] op_sel:[0,1] op_sel_hi:[1,0]
	ds_read2_b32 v[146:147], v145 offset0:71 offset1:72
	s_waitcnt lgkmcnt(0)
	v_pk_add_f32 v[112:113], v[112:113], v[146:147] op_sel:[0,1] op_sel_hi:[1,0]
	ds_read2_b32 v[146:147], v145 offset0:101 offset1:102
	s_waitcnt lgkmcnt(0)
	v_pk_add_f32 v[98:99], v[98:99], v[146:147] op_sel:[0,1] op_sel_hi:[1,0]
	ds_read2_b32 v[146:147], v145 offset0:69 offset1:70
	s_waitcnt lgkmcnt(0)
	v_pk_add_f32 v[114:115], v[114:115], v[146:147] op_sel:[0,1] op_sel_hi:[1,0]
.LBB0_1591:
	v_max3_f32 v145, v84, v85, v100
	v_max3_f32 v146, v86, v87, v101
	s_nop 0
	v_max3_f32 v145, v145, v102, v103
	v_max3_f32 v146, v146, v90, v91
	s_nop 0
	v_max3_f32 v145, v145, v88, v89
	v_max3_f32 v146, v146, v106, v107
	s_nop 0
	v_max3_f32 v145, v145, v104, v105
	v_max3_f32 v146, v146, v94, v95
	s_nop 0
	v_max3_f32 v145, v145, v92, v93
	v_max3_f32 v146, v146, v110, v111
	s_nop 0
	v_max3_f32 v145, v145, v108, v109
	v_max3_f32 v146, v146, v98, v99
	s_nop 0
	v_max3_f32 v145, v145, v96, v97
	v_max3_f32 v146, v146, v114, v115
	s_nop 0
	v_max3_f32 v145, v145, v112, v113
	s_nop 0
	v_max3_f32 v145, v145, v146, v146
	s_nop 0
	v_mov_b32_e32 v146, v145
	s_nop 1
	v_permlane32_swap_b32_e32 v145, v146
	v_max_f32_e32 v146, v146, v146
	v_max_f32_e32 v145, v145, v145
	v_max_f32_e32 v145, v145, v146
	v_add_f32_e32 v146, 0x40c00000, v2
	v_add_f32_e32 v147, 0, v145
	v_cmp_gt_f32_e32 vcc, v145, v146
	s_nop 1
	v_cndmask_b32_e32 v145, v2, v147, vcc
	v_cmp_gt_f32_e32 vcc, v145, v2
	s_cbranch_vccz .LBB0_1593
	v_sub_f32_e32 v2, v2, v145
	v_exp_f32_e32 v2, v2
	s_nop 0
	v_pk_mul_f32 v[66:67], v[66:67], v[2:3] op_sel_hi:[1,0]
	v_pk_mul_f32 v[64:65], v[64:65], v[2:3] op_sel_hi:[1,0]
	v_pk_mul_f32 v[62:63], v[62:63], v[2:3] op_sel_hi:[1,0]
	v_pk_mul_f32 v[60:61], v[60:61], v[2:3] op_sel_hi:[1,0]
	v_pk_mul_f32 v[58:59], v[58:59], v[2:3] op_sel_hi:[1,0]
	v_pk_mul_f32 v[56:57], v[56:57], v[2:3] op_sel_hi:[1,0]
	v_pk_mul_f32 v[54:55], v[54:55], v[2:3] op_sel_hi:[1,0]
	v_pk_mul_f32 v[52:53], v[52:53], v[2:3] op_sel_hi:[1,0]
	v_pk_mul_f32 v[34:35], v[34:35], v[2:3] op_sel_hi:[1,0]
	v_pk_mul_f32 v[32:33], v[32:33], v[2:3] op_sel_hi:[1,0]
	v_pk_mul_f32 v[30:31], v[30:31], v[2:3] op_sel_hi:[1,0]
	v_pk_mul_f32 v[28:29], v[28:29], v[2:3] op_sel_hi:[1,0]
	v_pk_mul_f32 v[26:27], v[26:27], v[2:3] op_sel_hi:[1,0]
	v_pk_mul_f32 v[24:25], v[24:25], v[2:3] op_sel_hi:[1,0]
	v_pk_mul_f32 v[22:23], v[22:23], v[2:3] op_sel_hi:[1,0]
	v_pk_mul_f32 v[20:21], v[20:21], v[2:3] op_sel_hi:[1,0]
	v_pk_mul_f32 v[18:19], v[18:19], v[2:3] op_sel_hi:[1,0]
	v_pk_mul_f32 v[16:17], v[16:17], v[2:3] op_sel_hi:[1,0]
	v_pk_mul_f32 v[14:15], v[14:15], v[2:3] op_sel_hi:[1,0]
	v_pk_mul_f32 v[12:13], v[12:13], v[2:3] op_sel_hi:[1,0]
	v_pk_mul_f32 v[10:11], v[10:11], v[2:3] op_sel_hi:[1,0]
	v_pk_mul_f32 v[8:9], v[8:9], v[2:3] op_sel_hi:[1,0]
	v_pk_mul_f32 v[6:7], v[6:7], v[2:3] op_sel_hi:[1,0]
	v_pk_mul_f32 v[4:5], v[4:5], v[2:3] op_sel_hi:[1,0]
